# v63 plus NA unit prologue/epilogue full waits relaxed to lgkmcnt only (K/V loads no longer wait for Q; next unit not blocked on stores)
# baseline (speedup 1.0000x reference)
.LBB0_874:
	s_lshl_b32 s76, s4, 7
	v_add_u32_e32 v192, s9, v178
	v_lshl_add_u64 v[194:195], v[182:183], 0, s[76:77]
	v_mad_i64_i32 v[0:1], s[2:3], v192, s59, v[194:195]
	v_add_u32_e32 v190, 16, v192
	global_load_dwordx4 v[56:59], v[0:1], off
	global_load_dwordx4 v[60:63], v[0:1], off offset:64
	v_mad_i64_i32 v[0:1], s[2:3], v190, s59, v[194:195]
	v_add_u32_e32 v188, 32, v192
	global_load_dwordx4 v[64:67], v[0:1], off
	global_load_dwordx4 v[68:71], v[0:1], off offset:64
	v_mad_i64_i32 v[0:1], s[2:3], v188, s59, v[194:195]
	v_add_u32_e32 v186, 48, v192
	global_load_dwordx4 v[72:75], v[0:1], off
	global_load_dwordx4 v[76:79], v[0:1], off offset:64
	v_mad_i64_i32 v[0:1], s[2:3], v186, s59, v[194:195]
	s_lshl_b32 s38, s6, 8
	global_load_dwordx4 v[80:83], v[0:1], off
	global_load_dwordx4 v[84:87], v[0:1], off offset:64
	v_add_u32_e32 v5, s38, v221
	v_mov_b64_e32 v[0:1], s[78:79]
	v_mad_i64_i32 v[2:3], s[2:3], v5, s59, v[0:1]
	v_lshl_add_u64 v[2:3], v[2:3], 0, s[76:77]
	v_lshlrev_b32_e32 v96, 1, v180
	v_lshl_add_u64 v[2:3], v[2:3], 0, v[96:97]
	s_waitcnt lgkmcnt(0)
	global_load_dwordx4 v[158:161], v[2:3], off offset:2048
	global_load_dwordx4 v[154:157], v[2:3], off offset:2112
	v_or_b32_e32 v2, 4, v5
	v_sub_u32_e64 v4, s7, 4 clamp
	v_mad_i64_i32 v[0:1], s[2:3], v2, s59, v[0:1]
	v_readfirstlane_b32 s2, v4
	s_lshl_b32 s34, s4, 6
	v_lshl_add_u64 v[0:1], v[0:1], 0, s[76:77]
	s_min_u32 s35, s2, 24
	s_mul_i32 s3, s6, 0x900
	v_lshl_add_u64 v[0:1], v[0:1], 0, v[96:97]
	s_add_u32 s3, s3, s34
	global_load_dwordx4 v[166:169], v[0:1], off offset:2048
	global_load_dwordx4 v[162:165], v[0:1], off offset:2112
	s_mul_hi_i32 s2, s6, 0x900
	v_mov_b32_e32 v2, s3
	v_mov_b64_e32 v[0:1], s[80:81]
	s_addc_u32 s4, s2, 0
	v_mad_u64_u32 v[196:197], s[2:3], v2, s75, v[0:1]
	v_mov_b32_e32 v0, 0x1200
	v_mad_i32_i24 v197, s4, v0, v197
	v_lshlrev_b32_e32 v0, 6, v178
	v_mov_b32_e32 v1, v97
	v_lshl_add_u64 v[196:197], v[196:197], 0, v[0:1]
	v_lshl_add_u64 v[0:1], v[196:197], 0, v[96:97]
	v_add_co_u32_e32 v2, vcc, 0x40000, v0
	s_mov_b32 s2, 0x40800
	s_nop 0
	v_addc_co_u32_e32 v3, vcc, 0, v1, vcc
	v_add_co_u32_e32 v4, vcc, s2, v0
	s_mov_b32 s2, 0x40c00
	s_nop 0
	v_addc_co_u32_e32 v5, vcc, 0, v1, vcc
	v_add_co_u32_e32 v6, vcc, s2, v0
	s_mov_b32 s2, 0x40400
	s_nop 0
	v_addc_co_u32_e32 v7, vcc, 0, v1, vcc
	v_add_co_u32_e32 v0, vcc, s2, v0
	global_load_dwordx4 v[110:113], v[4:5], off
	global_load_dwordx4 v[106:109], v[6:7], off
	v_addc_co_u32_e32 v1, vcc, 0, v1, vcc
	global_load_dwordx4 v[122:125], v[0:1], off
	global_load_dwordx4 v[134:137], v[2:3], off
	s_mov_b64 s[4:5], 0x400
	v_lshl_add_u64 v[198:199], v[196:197], 0, s[4:5]
	s_mov_b64 s[4:5], 0x800
	v_mov_b32_e32 v98, v97
	v_mov_b32_e32 v99, v97
	v_mov_b32_e32 v100, v97
	v_mov_b32_e32 v101, v97
	v_lshl_add_u64 v[200:201], v[196:197], 0, s[4:5]
	s_mov_b64 s[4:5], 0xc00
	s_lshl_b32 s37, s6, 11
	s_sub_i32 s39, s35, s7
	v_mov_b64_e32 v[104:105], v[100:101]
	v_mov_b64_e32 v[92:93], v[98:99]
	v_mov_b64_e32 v[88:89], v[98:99]
	v_mov_b64_e32 v[52:53], v[98:99]
	v_mov_b64_e32 v[48:49], v[98:99]
	v_mov_b64_e32 v[44:45], v[98:99]
	v_mov_b64_e32 v[40:41], v[98:99]
	v_mov_b64_e32 v[36:37], v[98:99]
	v_mov_b64_e32 v[32:33], v[98:99]
	v_mov_b64_e32 v[28:29], v[98:99]
	v_mov_b64_e32 v[24:25], v[98:99]
	v_mov_b64_e32 v[20:21], v[98:99]
	v_mov_b64_e32 v[16:17], v[98:99]
	v_mov_b64_e32 v[12:13], v[98:99]
	v_mov_b64_e32 v[8:9], v[98:99]
	v_ashrrev_i32_e32 v193, 31, v192
	v_ashrrev_i32_e32 v191, 31, v190
	s_mov_b32 s36, 32
	v_ashrrev_i32_e32 v189, 31, v188
	v_ashrrev_i32_e32 v187, 31, v186
	s_mov_b32 s2, 0
	v_lshl_add_u64 v[202:203], v[196:197], 0, s[4:5]
	s_addk_i32 s37, 0xff00
	s_addk_i32 s38, 0x2000
	s_add_i32 s39, s39, -4
	s_waitcnt vmcnt(7)
	v_mov_b64_e32 v[118:119], v[158:159]
	s_waitcnt vmcnt(6)
	v_mov_b64_e32 v[114:115], v[154:155]
	v_mov_b32_e32 v230, 0
	v_mov_b32_e32 v234, 0xf149f2ca
	v_mov_b32_e32 v235, 0xf149f2ca
	v_mov_b32_e32 v236, 0xf149f2ca
	v_mov_b32_e32 v237, 0xf149f2ca
	v_mov_b32_e32 v231, 0
	v_mov_b32_e32 v232, 0
	v_mov_b32_e32 v233, 0
	v_mov_b64_e32 v[102:103], v[98:99]
	v_mov_b64_e32 v[94:95], v[100:101]
	s_waitcnt vmcnt(5)
	v_mov_b64_e32 v[130:131], v[166:167]
	s_waitcnt vmcnt(4)
	v_mov_b64_e32 v[126:127], v[162:163]
	v_mov_b64_e32 v[90:91], v[100:101]
	v_mov_b64_e32 v[54:55], v[100:101]
	v_mov_b64_e32 v[50:51], v[100:101]
	v_mov_b64_e32 v[46:47], v[100:101]
	v_mov_b64_e32 v[42:43], v[100:101]
	v_mov_b64_e32 v[38:39], v[100:101]
	v_mov_b64_e32 v[34:35], v[100:101]
	v_mov_b64_e32 v[30:31], v[100:101]
	v_mov_b64_e32 v[26:27], v[100:101]
	v_mov_b64_e32 v[22:23], v[100:101]
	v_mov_b64_e32 v[18:19], v[100:101]
	v_mov_b64_e32 v[14:15], v[100:101]
	v_mov_b64_e32 v[10:11], v[100:101]
	v_mov_b64_e32 v[128:129], v[164:165]
	v_mov_b64_e32 v[132:133], v[168:169]
	v_mov_b64_e32 v[116:117], v[156:157]
	v_mov_b64_e32 v[120:121], v[160:161]
	s_waitcnt vmcnt(3)
	v_mov_b64_e32 v[152:153], v[112:113]
	s_waitcnt vmcnt(2)
	v_mov_b64_e32 v[148:149], v[108:109]
	v_mov_b64_e32 v[146:147], v[106:107]
	s_waitcnt vmcnt(1)
	v_mov_b64_e32 v[140:141], v[124:125]
	s_waitcnt vmcnt(0)
	v_mov_b64_e32 v[144:145], v[136:137]
	v_mov_b64_e32 v[150:151], v[110:111]
	v_mov_b64_e32 v[138:139], v[122:123]
	v_mov_b64_e32 v[142:143], v[134:135]
	s_add_i32 s40, s2, 1
	s_cmp_ge_u32 s40, s31
	s_cbranch_scc1 .LBB0_877
	s_branch .LBB0_876

.LBB0_905:
	v_add_f32_e32 v0, v170, v171
	v_add_f32_e32 v1, v172, v173
	v_add_f32_e32 v0, v0, v1
	v_add_f32_e32 v1, v174, v175
	v_add_f32_e32 v2, v176, v177
	v_add_f32_e32 v1, v1, v2
	v_add_f32_e32 v0, v0, v1
	v_add_f32_e32 v231, v0, v231
	v_add_f32_e32 v0, v238, v239
	v_add_f32_e32 v1, v240, v241
	v_add_f32_e32 v0, v0, v1
	v_add_f32_e32 v1, v242, v243
	v_add_f32_e32 v2, v244, v245
	v_add_f32_e32 v1, v1, v2
	v_add_f32_e32 v0, v0, v1
	s_add_i32 s36, s36, 32
	s_cmp_eq_u32 s31, s40
	v_add_f32_e32 v232, v0, v232
	s_cbranch_scc0 .LBB0_875
	ds_swizzle_b32 v2, v233 offset:swizzle(SWAP,16)
	s_lshl_b32 s76, s34, 1
	v_lshl_add_u64 v[0:1], v[184:185], 0, s[76:77]
	s_and_b64 s[2:3], exec, s[24:25]
	s_cselect_b32 s8, s29, s28
	s_waitcnt lgkmcnt(0)
	v_add_f32_e32 v2, v233, v2
	v_mov_b32_e32 v3, v2
	s_nop 1
	v_permlane32_swap_b32_e32 v2, v3
	v_add_f32_e32 v2, v2, v3
	v_div_scale_f32 v3, s[2:3], v2, v2, 1.0
	v_rcp_f32_e32 v4, v3
	s_cmp_ge_i32 s8, s29
	v_fma_f32 v5, -v3, v4, 1.0
	v_fmac_f32_e32 v4, v5, v4
	v_div_scale_f32 v5, vcc, 1.0, v2, 1.0
	v_mul_f32_e32 v6, v5, v4
	v_fma_f32 v7, -v3, v6, v5
	v_fmac_f32_e32 v6, v7, v4
	v_fma_f32 v3, -v3, v6, v5
	v_div_fmas_f32 v3, v3, v4, v6
	v_div_fixup_f32 v2, v3, v2, 1.0
	v_lshlrev_b64 v[4:5], 11, v[192:193]
	v_pk_mul_f32 v[6:7], v[100:101], v[2:3] op_sel_hi:[1,0]
	v_pk_mul_f32 v[56:57], v[98:99], v[2:3] op_sel_hi:[1,0]
	v_lshl_add_u64 v[4:5], v[0:1], 0, v[4:5]
	v_cvt_pk_bf16_f32 v56, v56, v57
	v_cvt_pk_bf16_f32 v57, v6, v7
	global_store_dwordx2 v[4:5], v[56:57], off
	v_pk_mul_f32 v[6:7], v[104:105], v[2:3] op_sel_hi:[1,0]
	v_pk_mul_f32 v[56:57], v[102:103], v[2:3] op_sel_hi:[1,0]
	s_nop 0
	v_cvt_pk_bf16_f32 v56, v56, v57
	v_cvt_pk_bf16_f32 v57, v6, v7
	global_store_dwordx2 v[4:5], v[56:57], off offset:32
	v_pk_mul_f32 v[6:7], v[94:95], v[2:3] op_sel_hi:[1,0]
	v_pk_mul_f32 v[56:57], v[92:93], v[2:3] op_sel_hi:[1,0]
	s_nop 0
	v_cvt_pk_bf16_f32 v56, v56, v57
	v_cvt_pk_bf16_f32 v57, v6, v7
	v_pk_mul_f32 v[6:7], v[90:91], v[2:3] op_sel_hi:[1,0]
	v_pk_mul_f32 v[2:3], v[88:89], v[2:3] op_sel_hi:[1,0]
	global_store_dwordx2 v[4:5], v[56:57], off offset:64
	v_cvt_pk_bf16_f32 v2, v2, v3
	v_cvt_pk_bf16_f32 v3, v6, v7
	global_store_dwordx2 v[4:5], v[2:3], off offset:96
	ds_swizzle_b32 v2, v232 offset:swizzle(SWAP,16)
	s_waitcnt lgkmcnt(0)
	v_add_f32_e32 v2, v232, v2
	v_mov_b32_e32 v3, v2
	s_nop 1
	v_permlane32_swap_b32_e32 v2, v3
	v_add_f32_e32 v2, v2, v3
	v_div_scale_f32 v3, s[2:3], v2, v2, 1.0
	v_rcp_f32_e32 v4, v3
	s_nop 0
	v_fma_f32 v5, -v3, v4, 1.0
	v_fmac_f32_e32 v4, v5, v4
	v_div_scale_f32 v5, vcc, 1.0, v2, 1.0
	v_mul_f32_e32 v6, v5, v4
	v_fma_f32 v7, -v3, v6, v5
	v_fmac_f32_e32 v6, v7, v4
	v_fma_f32 v3, -v3, v6, v5
	v_div_fmas_f32 v3, v3, v4, v6
	v_div_fixup_f32 v2, v3, v2, 1.0
	v_pk_mul_f32 v[6:7], v[54:55], v[2:3] op_sel_hi:[1,0]
	v_pk_mul_f32 v[52:53], v[52:53], v[2:3] op_sel_hi:[1,0]
	v_pk_mul_f32 v[48:49], v[48:49], v[2:3] op_sel_hi:[1,0]
	v_cvt_pk_bf16_f32 v52, v52, v53
	v_cvt_pk_bf16_f32 v53, v6, v7
	v_pk_mul_f32 v[6:7], v[50:51], v[2:3] op_sel_hi:[1,0]
	v_cvt_pk_bf16_f32 v48, v48, v49
	v_cvt_pk_bf16_f32 v49, v6, v7
	v_pk_mul_f32 v[6:7], v[46:47], v[2:3] op_sel_hi:[1,0]
	v_pk_mul_f32 v[44:45], v[44:45], v[2:3] op_sel_hi:[1,0]
	v_lshlrev_b64 v[4:5], 11, v[190:191]
	v_cvt_pk_bf16_f32 v44, v44, v45
	v_cvt_pk_bf16_f32 v45, v6, v7
	v_pk_mul_f32 v[6:7], v[42:43], v[2:3] op_sel_hi:[1,0]
	v_pk_mul_f32 v[2:3], v[40:41], v[2:3] op_sel_hi:[1,0]
	v_lshl_add_u64 v[4:5], v[0:1], 0, v[4:5]
	v_cvt_pk_bf16_f32 v2, v2, v3
	v_cvt_pk_bf16_f32 v3, v6, v7
	global_store_dwordx2 v[4:5], v[2:3], off offset:96
	ds_swizzle_b32 v2, v231 offset:swizzle(SWAP,16)
	global_store_dwordx2 v[4:5], v[52:53], off
	global_store_dwordx2 v[4:5], v[48:49], off offset:32
	global_store_dwordx2 v[4:5], v[44:45], off offset:64
	s_waitcnt lgkmcnt(0)
	v_add_f32_e32 v2, v231, v2
	v_mov_b32_e32 v3, v2
	s_nop 1
	v_permlane32_swap_b32_e32 v2, v3
	v_add_f32_e32 v2, v2, v3
	v_div_scale_f32 v3, s[2:3], v2, v2, 1.0
	v_rcp_f32_e32 v4, v3
	s_nop 0
	v_fma_f32 v5, -v3, v4, 1.0
	v_fmac_f32_e32 v4, v5, v4
	v_div_scale_f32 v5, vcc, 1.0, v2, 1.0
	v_mul_f32_e32 v6, v5, v4
	v_fma_f32 v7, -v3, v6, v5
	v_fmac_f32_e32 v6, v7, v4
	v_fma_f32 v3, -v3, v6, v5
	v_div_fmas_f32 v3, v3, v4, v6
	v_div_fixup_f32 v2, v3, v2, 1.0
	v_pk_mul_f32 v[6:7], v[38:39], v[2:3] op_sel_hi:[1,0]
	v_pk_mul_f32 v[36:37], v[36:37], v[2:3] op_sel_hi:[1,0]
	v_pk_mul_f32 v[32:33], v[32:33], v[2:3] op_sel_hi:[1,0]
	v_cvt_pk_bf16_f32 v36, v36, v37
	v_cvt_pk_bf16_f32 v37, v6, v7
	v_pk_mul_f32 v[6:7], v[34:35], v[2:3] op_sel_hi:[1,0]
	v_cvt_pk_bf16_f32 v32, v32, v33
	v_cvt_pk_bf16_f32 v33, v6, v7
	v_pk_mul_f32 v[6:7], v[30:31], v[2:3] op_sel_hi:[1,0]
	v_pk_mul_f32 v[28:29], v[28:29], v[2:3] op_sel_hi:[1,0]
	v_lshlrev_b64 v[4:5], 11, v[188:189]
	v_cvt_pk_bf16_f32 v28, v28, v29
	v_cvt_pk_bf16_f32 v29, v6, v7
	v_pk_mul_f32 v[6:7], v[26:27], v[2:3] op_sel_hi:[1,0]
	v_pk_mul_f32 v[2:3], v[24:25], v[2:3] op_sel_hi:[1,0]
	v_lshl_add_u64 v[4:5], v[0:1], 0, v[4:5]
	v_cvt_pk_bf16_f32 v2, v2, v3
	v_cvt_pk_bf16_f32 v3, v6, v7
	global_store_dwordx2 v[4:5], v[2:3], off offset:96
	ds_swizzle_b32 v2, v230 offset:swizzle(SWAP,16)
	global_store_dwordx2 v[4:5], v[36:37], off
	global_store_dwordx2 v[4:5], v[32:33], off offset:32
	global_store_dwordx2 v[4:5], v[28:29], off offset:64
	s_waitcnt lgkmcnt(0)
	v_add_f32_e32 v2, v230, v2
	v_mov_b32_e32 v3, v2
	s_nop 1
	v_permlane32_swap_b32_e32 v2, v3
	v_add_f32_e32 v2, v2, v3
	v_div_scale_f32 v3, s[2:3], v2, v2, 1.0
	v_rcp_f32_e32 v4, v3
	s_nop 0
	v_fma_f32 v5, -v3, v4, 1.0
	v_fmac_f32_e32 v4, v5, v4
	v_div_scale_f32 v5, vcc, 1.0, v2, 1.0
	v_mul_f32_e32 v6, v5, v4
	v_fma_f32 v7, -v3, v6, v5
	v_fmac_f32_e32 v6, v7, v4
	v_fma_f32 v3, -v3, v6, v5
	v_div_fmas_f32 v3, v3, v4, v6
	v_div_fixup_f32 v2, v3, v2, 1.0
	v_lshlrev_b64 v[4:5], 11, v[186:187]
	v_lshl_add_u64 v[0:1], v[0:1], 0, v[4:5]
	v_pk_mul_f32 v[4:5], v[22:23], v[2:3] op_sel_hi:[1,0]
	v_pk_mul_f32 v[6:7], v[20:21], v[2:3] op_sel_hi:[1,0]
	s_nop 0
	v_cvt_pk_bf16_f32 v6, v6, v7
	v_cvt_pk_bf16_f32 v7, v4, v5
	global_store_dwordx2 v[0:1], v[6:7], off
	v_pk_mul_f32 v[4:5], v[18:19], v[2:3] op_sel_hi:[1,0]
	v_pk_mul_f32 v[6:7], v[16:17], v[2:3] op_sel_hi:[1,0]
	s_nop 0
	v_cvt_pk_bf16_f32 v6, v6, v7
	v_cvt_pk_bf16_f32 v7, v4, v5
	global_store_dwordx2 v[0:1], v[6:7], off offset:32
	v_pk_mul_f32 v[4:5], v[14:15], v[2:3] op_sel_hi:[1,0]
	v_pk_mul_f32 v[6:7], v[12:13], v[2:3] op_sel_hi:[1,0]
	s_nop 0
	v_cvt_pk_bf16_f32 v6, v6, v7
	v_cvt_pk_bf16_f32 v7, v4, v5
	v_pk_mul_f32 v[4:5], v[10:11], v[2:3] op_sel_hi:[1,0]
	v_pk_mul_f32 v[2:3], v[8:9], v[2:3] op_sel_hi:[1,0]
	global_store_dwordx2 v[0:1], v[6:7], off offset:64
	v_cvt_pk_bf16_f32 v2, v2, v3
	v_cvt_pk_bf16_f32 v3, v4, v5
	global_store_dwordx2 v[0:1], v[2:3], off offset:96
	s_waitcnt lgkmcnt(0)
	s_cbranch_scc0 .LBB0_866
